# MFMA shadow fill: accumulator-clearing MFMAs interleaved with the scalar tile-map chain in the FFN-up unit-loop headers (stub on the no-next-unit path)
# baseline (speedup 1.0000x reference)
;     DI bool next(int i, Unit& u) const { u.aux = 0; return tile_map(i, nM, nN, G, c, u.pm, u.pn); }
;     DI size_t a_off(const Unit& u) const { return (size_t)u.pm * astep; }
;     DI size_t b_off(const Unit& u) const { return (size_t)u.pn * bstep; }
;     DI bool next(int i, Unit& u) const { int pn; u.aux = 0; if (!tile_map(i, NTOK / 256, 16, G, c, u.pm, pn)) return false; u.pn = pn < 8 ? pn : pn + 8; return true; }
;     DI size_t a_off(const Unit& u) const { return (size_t)u.pm * (256 * D_ * 2); }
;     DI size_t b_off(const Unit& u) const { return (size_t)u.pn * (256 * D_ * 2); }
;     DI bool next(int i, Unit& u) const { int pn2; if (!tile_map(i, NTOK / 256, 8, G, c, u.pm, pn2)) return false; u.pn = pn2 >> 1; u.aux = pn2 & 1; return true; }
;     DI size_t a_off(const Unit& u) const { return (size_t)u.pm * (256 * D_ * 2) + (size_t)u.aux * (D_ / 2 * 2); }
;     DI size_t b_off(const Unit& u) const { return (size_t)(12 + u.pn) * (256 * D_ * 2) + (size_t)u.aux * (D_ / 2 * 2); }
;     DI bool next(int i, Unit& u) const { u.aux = 0; return tile_map(i, 8, NTOK / 256, G, c, u.pm, u.pn); }
;     DI size_t b_off(const Unit& u) const { return (size_t)u.pn * (256 * D_ * 2); }
; DI bool tile_map(int i, int nM, int nN, int G, int c, int& pm, int& pn) {
;     const int nwg = nM * nN; const long L = (long)i * G + c; if (L >= nwg) return false;
;     int wgid = (int)L; { const int q = nwg / NXCD, r = nwg % NXCD, xcd = wgid % NXCD, off = wgid / NXCD; wgid = (xcd < r ? xcd * (q + 1) : r * (q + 1) + (xcd - r) * q) + off; }
;     const int nig = WGM * nN, gid = wgid / nig, fm = gid * WGM, gsz = (nM - fm) < WGM ? (nM - fm) : WGM;
;     pm = fm + ((wgid % nig) % gsz); pn = (wgid % nig) / gsz; return true;
; template <class Epi, class Sched, bool ALIGN_EPI, bool FP8 = false>
; DI void gemm_phase(LAS unsigned char* lds, const Gemm g, const Sched& S, const Epi& E) {
;     ...
;     for (;;) {
;         const bool has_next = S.next(ui + 1, nxt);
;         const char* nA = has_next ? (const char*)g.A + S.a_off(nxt) : cA; const char* nB = has_next ? (const char*)g.Bt + S.b_off(nxt) : cB;
;     ...
; #pragma unroll
;         for (int a = 0; a < 2; ++a)
; #pragma unroll
;             for (int b = 0; b < 2; ++b)
; #pragma unroll
;                 for (int m = 0; m < 4; ++m)
; #pragma unroll
;                     for (int n = 0; n < 2; ++n) acc[a][b][m][n] = (f32x4){0.f, 0.f, 0.f, 0.f};
.LBB0_697:
	v_mov_b32_e32 v124, 0
	v_mov_b32_e32 v125, 0
	v_mov_b32_e32 v126, 0
	v_mov_b32_e32 v127, 0
	s_nop 1
	v_mfma_f32_32x32x16_bf16 v[0:15], v[124:127], v[124:127], 0
	v_mfma_f32_32x32x16_bf16 v[16:31], v[124:127], v[124:127], 0
	s_add_i32 s39, s39, 1
	s_mul_i32 s4, s39, s63
	s_mul_hi_u32 s5, s39, s34
	s_add_i32 s5, s5, s4
	s_mul_i32 s4, s39, s34
	s_add_u32 s18, s4, s2
	s_addc_u32 s19, s5, s45
	v_cmp_gt_i64_e32 vcc, s[18:19], v[130:131]
	v_cmp_lt_i64_e64 s[4:5], s[18:19], v[128:129]
	s_cbranch_vccnz .Lmy_zs_1
	s_ashr_i32 s12, s18, 31
	s_lshr_b32 s12, s12, 29
	s_add_i32 s12, s18, s12
	s_ashr_i32 s13, s12, 3
	s_and_b32 s12, s12, -8
	s_sub_i32 s12, s18, s12
	v_mfma_f32_32x32x16_bf16 v[32:47], v[124:127], v[124:127], 0
	s_cmp_lt_i32 s12, 0
	s_cselect_b32 s16, s46, 0xb0
	s_mul_i32 s12, s16, s12
	s_add_i32 s12, s12, s13
	s_mul_hi_i32 s13, s12, 0x2e8ba2e9
	s_lshr_b32 s16, s13, 31
	v_mfma_f32_32x32x16_bf16 v[48:63], v[124:127], v[124:127], 0
	s_ashr_i32 s13, s13, 6
	s_add_i32 s13, s13, s16
	s_lshl_b32 s16, s13, 3
	s_sub_i32 s17, 32, s16
	s_min_i32 s17, s17, 8
	s_abs_i32 s18, s17
	v_mfma_f32_32x32x16_bf16 v[64:79], v[124:127], v[124:127], 0
	v_cvt_f32_u32_e32 v255, s18
	s_sub_i32 s20, 0, s18
	s_mulk_i32 s13, 0x160
	s_sub_i32 s13, s12, s13
	v_rcp_iflag_f32_e32 v255, v255
	s_abs_i32 s12, s13
	v_mfma_f32_32x32x16_bf16 v[80:95], v[124:127], v[124:127], 0
	s_xor_b32 s19, s13, s17
	s_ashr_i32 s19, s19, 31
	v_mul_f32_e32 v255, 0x4f7ffffe, v255
	v_cvt_u32_f32_e32 v255, v255
	s_nop 0
	v_readfirstlane_b32 s21, v255
	v_mfma_f32_32x32x16_bf16 v[96:111], v[124:127], v[124:127], 0
	s_mul_i32 s20, s20, s21
	s_mul_hi_u32 s20, s21, s20
	s_add_i32 s21, s21, s20
	s_mul_hi_u32 s20, s12, s21
	s_mul_i32 s21, s20, s18
	s_sub_i32 s12, s12, s21
	v_mfma_f32_16x16x32_bf16 v[112:115], v[124:127], v[124:127], 0
	s_add_i32 s28, s20, 1
	s_sub_i32 s21, s12, s18
	s_cmp_ge_u32 s12, s18
	s_cselect_b32 s20, s28, s20
	s_cselect_b32 s12, s21, s12
	s_add_i32 s21, s20, 1
	v_mfma_f32_16x16x32_bf16 v[116:119], v[124:127], v[124:127], 0
	s_cmp_ge_u32 s12, s18
	s_cselect_b32 s12, s21, s20
	s_xor_b32 s12, s12, s19
	s_sub_i32 s12, s12, s19
	s_mul_i32 s17, s12, s17
	s_sub_i32 s13, s13, s17
	v_mfma_f32_16x16x32_bf16 v[120:123], v[124:127], v[124:127], 0
	s_add_i32 s16, s13, s16
	s_branch .LBB0_699
.Lmy_zs_1:
	v_mfma_f32_32x32x16_bf16 v[32:47], v[124:127], v[124:127], 0
	v_mfma_f32_32x32x16_bf16 v[48:63], v[124:127], v[124:127], 0
	v_mfma_f32_32x32x16_bf16 v[64:79], v[124:127], v[124:127], 0
	v_mfma_f32_32x32x16_bf16 v[80:95], v[124:127], v[124:127], 0
	v_mfma_f32_32x32x16_bf16 v[96:111], v[124:127], v[124:127], 0
	v_mfma_f32_16x16x32_bf16 v[112:115], v[124:127], v[124:127], 0
	v_mfma_f32_16x16x32_bf16 v[116:119], v[124:127], v[124:127], 0
	v_mfma_f32_16x16x32_bf16 v[120:123], v[124:127], v[124:127], 0

;     DI bool next(int i, Unit& u) const { u.aux = 0; return tile_map(i, nM, nN, G, c, u.pm, u.pn); }
;     DI size_t a_off(const Unit& u) const { return (size_t)u.pm * astep; }
;     DI size_t b_off(const Unit& u) const { return (size_t)u.pn * bstep; }
;     DI bool next(int i, Unit& u) const { int pn; u.aux = 0; if (!tile_map(i, NTOK / 256, 16, G, c, u.pm, pn)) return false; u.pn = pn < 8 ? pn : pn + 8; return true; }
;     DI size_t a_off(const Unit& u) const { return (size_t)u.pm * (256 * D_ * 2); }
;     DI size_t b_off(const Unit& u) const { return (size_t)u.pn * (256 * D_ * 2); }
;     DI bool next(int i, Unit& u) const { int pn2; if (!tile_map(i, NTOK / 256, 8, G, c, u.pm, pn2)) return false; u.pn = pn2 >> 1; u.aux = pn2 & 1; return true; }
;     DI size_t a_off(const Unit& u) const { return (size_t)u.pm * (256 * D_ * 2) + (size_t)u.aux * (D_ / 2 * 2); }
;     DI size_t b_off(const Unit& u) const { return (size_t)(12 + u.pn) * (256 * D_ * 2) + (size_t)u.aux * (D_ / 2 * 2); }
;     DI bool next(int i, Unit& u) const { u.aux = 0; return tile_map(i, 8, NTOK / 256, G, c, u.pm, u.pn); }
;     DI size_t a_off(const Unit& u) const { const int phys = u.pm < 4 ? 8 + u.pm : 20 + u.pm; return (size_t)phys * (256 * D_ * 2); }
;     DI size_t b_off(const Unit& u) const { return (size_t)u.pn * (256 * D_ * 2); }
; DI bool tile_map(int i, int nM, int nN, int G, int c, int& pm, int& pn) {
;     const int nwg = nM * nN; const long L = (long)i * G + c; if (L >= nwg) return false;
;     int wgid = (int)L; { const int q = nwg / NXCD, r = nwg % NXCD, xcd = wgid % NXCD, off = wgid / NXCD; wgid = (xcd < r ? xcd * (q + 1) : r * (q + 1) + (xcd - r) * q) + off; }
;     const int nig = WGM * nN, gid = wgid / nig, fm = gid * WGM, gsz = (nM - fm) < WGM ? (nM - fm) : WGM;
;     pm = fm + ((wgid % nig) % gsz); pn = (wgid % nig) / gsz; return true;
; template <class Epi, class Sched, bool ALIGN_EPI, bool FP8 = false>
; DI void gemm_phase(LAS unsigned char* lds, const Gemm g, const Sched& S, const Epi& E) {
;     ...
;     for (;;) {
;         const bool has_next = S.next(ui + 1, nxt);
;         const char* nA = has_next ? (const char*)g.A + S.a_off(nxt) : cA; const char* nB = has_next ? (const char*)g.Bt + S.b_off(nxt) : cB;
;     DI bool next(int i, Unit& u) const { if (!tile_map(i, nM, nN, G, c, u.pm, u.pn)) return false; u.aux = __builtin_amdgcn_readfirstlane(blk_e[u.pm]); return true; }
.LBB0_1603:
	v_mov_b32_e32 v124, 0
	v_mov_b32_e32 v125, 0
	v_mov_b32_e32 v126, 0
	v_mov_b32_e32 v127, 0
	s_nop 1
	v_mfma_f32_32x32x16_bf16 v[0:15], v[124:127], v[124:127], 0
	v_mfma_f32_32x32x16_bf16 v[16:31], v[124:127], v[124:127], 0
	s_add_i32 s55, s55, 1
	s_mul_i32 s4, s55, s64
	s_mul_hi_u32 s5, s55, s34
	s_add_i32 s5, s5, s4
	s_mul_i32 s4, s55, s34
	s_add_u32 s4, s4, s2
	s_addc_u32 s5, s5, s46
	v_cmp_ge_i64_e32 vcc, s[4:5], v[252:253]
	v_cmp_lt_i64_e64 s[6:7], s[4:5], v[252:253]
	s_cbranch_vccnz .Lmy_zs_0
	s_ashr_i32 s5, s4, 31
	s_lshr_b32 s5, s5, 29
	s_add_i32 s5, s4, s5
	s_ashr_i32 s14, s5, 3
	s_and_b32 s5, s5, -8
	s_sub_i32 s4, s4, s5
	v_mfma_f32_32x32x16_bf16 v[32:47], v[124:127], v[124:127], 0
	s_cmp_lt_i32 s4, 0
	s_cselect_b32 s5, s47, s45
	s_mul_i32 s4, s5, s4
	s_add_i32 s4, s4, s14
	s_mul_hi_i32 s5, s4, 0x92492493
	s_add_i32 s5, s5, s4
	v_mfma_f32_32x32x16_bf16 v[48:63], v[124:127], v[124:127], 0
	s_lshr_b32 s14, s5, 31
	s_ashr_i32 s5, s5, 8
	s_add_i32 s5, s5, s14
	s_lshl_b32 s15, s5, 3
	s_sub_i32 s14, s3, s15
	s_min_i32 s16, s14, 8
	v_mfma_f32_32x32x16_bf16 v[64:79], v[124:127], v[124:127], 0
	s_abs_i32 s14, s16
	v_cvt_f32_u32_e32 v255, s14
	s_sub_i32 s18, 0, s14
	s_mulk_i32 s5, 0x1c0
	s_sub_i32 s4, s4, s5
	v_rcp_iflag_f32_e32 v255, v255
	v_mfma_f32_32x32x16_bf16 v[80:95], v[124:127], v[124:127], 0
	s_abs_i32 s5, s4
	s_xor_b32 s17, s4, s16
	s_ashr_i32 s17, s17, 31
	v_mul_f32_e32 v255, 0x4f7ffffe, v255
	v_cvt_u32_f32_e32 v255, v255
	s_nop 0
	v_readfirstlane_b32 s19, v255
	v_mfma_f32_32x32x16_bf16 v[96:111], v[124:127], v[124:127], 0
	s_mul_i32 s18, s18, s19
	s_mul_hi_u32 s18, s19, s18
	s_add_i32 s19, s19, s18
	s_mul_hi_u32 s18, s5, s19
	s_mul_i32 s19, s18, s14
	s_sub_i32 s5, s5, s19
	v_mfma_f32_16x16x32_bf16 v[112:115], v[124:127], v[124:127], 0
	s_add_i32 s20, s18, 1
	s_sub_i32 s19, s5, s14
	s_cmp_ge_u32 s5, s14
	s_cselect_b32 s18, s20, s18
	s_cselect_b32 s5, s19, s5
	s_add_i32 s19, s18, 1
	v_mfma_f32_16x16x32_bf16 v[116:119], v[124:127], v[124:127], 0
	s_cmp_ge_u32 s5, s14
	s_cselect_b32 s5, s19, s18
	s_xor_b32 s5, s5, s17
	s_sub_i32 s14, s5, s17
	s_mul_i32 s5, s14, s16
	s_sub_i32 s4, s4, s5
	v_mfma_f32_16x16x32_bf16 v[120:123], v[124:127], v[124:127], 0
	s_add_i32 s16, s4, s15
	s_lshl_b32 s4, s16, 2
	s_add_i32 s4, s4, 0
	s_add_i32 s4, s4, 0x20400
	v_mov_b32_e32 v255, s4
	ds_read_b32 v255, v255
	s_waitcnt lgkmcnt(0)
	v_readfirstlane_b32 s67, v255
	s_branch .LBB0_1605
